# P1 GEMM load segments: 8 of 16 LDS-DMA loads per iteration take the saddr form (SGPR pair + 32-bit lane offset), their 64-bit VALU address adds removed; on top of v114
# speedup vs baseline: 1.0048x; 1.0048x over previous
.LBB0_389:
	s_add_u32 s0, s30, 0xfffc0080
	s_addc_u32 s1, s31, -1
	s_add_i32 s33, 0, 0x10000
	s_cmp_eq_u32 s79, 12
	s_cselect_b32 s67, s7, s1
	s_cselect_b32 s66, s9, s0
	s_cselect_b32 s65, s23, s78
	s_cselect_b32 s64, s25, s77
	s_add_i32 m0, s40, 0xc000
	ds_read_b128 v[174:177], v161
	ds_read_b128 v[178:181], v161 offset:1024
	ds_read_b128 v[182:185], v161 offset:2048
	ds_read_b128 v[186:189], v161 offset:3072
	ds_read_b128 v[190:193], v161 offset:4096
	ds_read_b128 v[198:201], v161 offset:5120
	ds_read_b128 v[202:205], v161 offset:6144
	ds_read_b128 v[206:209], v161 offset:7168
	global_load_lds_dwordx4 v148, s[30:31]
	s_add_i32 m0, s40, 0xe000
	s_nop 0
	global_load_lds_dwordx4 v150, s[30:31]
	s_waitcnt lgkmcnt(8)
	s_barrier
	s_waitcnt lgkmcnt(0)
	v_mfma_f32_16x16x32_bf16 v[126:129], v[152:155], v[174:177], v[126:129]
	v_mfma_f32_16x16x32_bf16 v[122:125], v[166:169], v[174:177], v[122:125]
	v_mfma_f32_16x16x32_bf16 v[110:113], v[152:155], v[182:185], v[110:113]
	v_mfma_f32_16x16x32_bf16 v[106:109], v[166:169], v[182:185], v[106:109]
	v_mfma_f32_16x16x32_bf16 v[94:97], v[152:155], v[190:193], v[94:97]
	v_mfma_f32_16x16x32_bf16 v[90:93], v[166:169], v[190:193], v[90:93]
	v_mfma_f32_16x16x32_bf16 v[78:81], v[152:155], v[202:205], v[78:81]
	v_mfma_f32_16x16x32_bf16 v[74:77], v[166:169], v[202:205], v[74:77]
	v_mfma_f32_16x16x32_bf16 v[126:129], v[162:165], v[178:181], v[126:129]
	v_mfma_f32_16x16x32_bf16 v[122:125], v[170:173], v[178:181], v[122:125]
	v_mfma_f32_16x16x32_bf16 v[110:113], v[162:165], v[186:189], v[110:113]
	v_mfma_f32_16x16x32_bf16 v[106:109], v[170:173], v[186:189], v[106:109]
	v_mfma_f32_16x16x32_bf16 v[94:97], v[162:165], v[198:201], v[94:97]
	v_mfma_f32_16x16x32_bf16 v[90:93], v[170:173], v[198:201], v[90:93]
	v_mfma_f32_16x16x32_bf16 v[78:81], v[162:165], v[206:209], v[78:81]
	v_mfma_f32_16x16x32_bf16 v[74:77], v[170:173], v[206:209], v[74:77]
	s_barrier
	s_add_i32 s36, 0, 0x14000
	v_add_u32_e32 v156, s36, v158
	s_add_i32 s0, s33, s38
	ds_read_b128 v[210:213], v156
	ds_read_b128 v[214:217], v156 offset:1024
	ds_read_b128 v[218:221], v156 offset:2048
	ds_read_b128 v[238:241], v156 offset:3072
	v_lshl_add_u64 v[156:157], s[64:65], 0, v[132:133]
	s_mov_b32 m0, s0
	v_lshl_add_u64 v[242:243], s[64:65], 0, v[136:137]
	global_load_lds_dwordx4 v[156:157], off
	s_add_i32 m0, s0, 0x2000
	s_nop 0
	global_load_lds_dwordx4 v[242:243], off
	s_barrier
	s_waitcnt lgkmcnt(0)
	v_mfma_f32_16x16x32_bf16 v[118:121], v[210:213], v[174:177], v[118:121]
	v_mfma_f32_16x16x32_bf16 v[114:117], v[218:221], v[174:177], v[114:117]
	v_mfma_f32_16x16x32_bf16 v[102:105], v[210:213], v[182:185], v[102:105]
	v_mfma_f32_16x16x32_bf16 v[98:101], v[218:221], v[182:185], v[98:101]
	v_mfma_f32_16x16x32_bf16 v[86:89], v[210:213], v[190:193], v[86:89]
	v_mfma_f32_16x16x32_bf16 v[82:85], v[218:221], v[190:193], v[82:85]
	v_mfma_f32_16x16x32_bf16 v[70:73], v[210:213], v[202:205], v[70:73]
	v_mfma_f32_16x16x32_bf16 v[66:69], v[218:221], v[202:205], v[66:69]
	v_mfma_f32_16x16x32_bf16 v[118:121], v[214:217], v[178:181], v[118:121]
	v_mfma_f32_16x16x32_bf16 v[114:117], v[238:241], v[178:181], v[114:117]
	v_mfma_f32_16x16x32_bf16 v[102:105], v[214:217], v[186:189], v[102:105]
	v_mfma_f32_16x16x32_bf16 v[98:101], v[238:241], v[186:189], v[98:101]
	v_mfma_f32_16x16x32_bf16 v[86:89], v[214:217], v[198:201], v[86:89]
	v_mfma_f32_16x16x32_bf16 v[82:85], v[238:241], v[198:201], v[82:85]
	v_mfma_f32_16x16x32_bf16 v[70:73], v[214:217], v[206:209], v[70:73]
	v_mfma_f32_16x16x32_bf16 v[66:69], v[238:241], v[206:209], v[66:69]
	s_mov_b32 m0, s40
	v_lshl_add_u64 v[244:245], s[66:67], 0, v[130:131]
	s_barrier
	ds_read_b128 v[174:177], v161 offset:16384
	ds_read_b128 v[178:181], v161 offset:17408
	ds_read_b128 v[182:185], v161 offset:18432
	ds_read_b128 v[186:189], v161 offset:19456
	ds_read_b128 v[190:193], v161 offset:20480
	ds_read_b128 v[198:201], v161 offset:21504
	ds_read_b128 v[202:205], v161 offset:22528
	ds_read_b128 v[206:209], v161 offset:23552
	global_load_lds_dwordx4 v[244:245], off
	v_lshl_add_u64 v[246:247], s[66:67], 0, v[134:135]
	s_mov_b32 m0, s43
	s_nop 0
	global_load_lds_dwordx4 v[246:247], off
	s_waitcnt vmcnt(10)
	s_barrier
	s_waitcnt lgkmcnt(0)
	v_mfma_f32_16x16x32_bf16 v[62:65], v[152:155], v[174:177], v[62:65]
	v_mfma_f32_16x16x32_bf16 v[58:61], v[166:169], v[174:177], v[58:61]
	v_mfma_f32_16x16x32_bf16 v[46:49], v[152:155], v[182:185], v[46:49]
	v_mfma_f32_16x16x32_bf16 v[42:45], v[166:169], v[182:185], v[42:45]
	v_mfma_f32_16x16x32_bf16 v[30:33], v[152:155], v[190:193], v[30:33]
	v_mfma_f32_16x16x32_bf16 v[26:29], v[166:169], v[190:193], v[26:29]
	v_mfma_f32_16x16x32_bf16 v[14:17], v[152:155], v[202:205], v[14:17]
	v_mfma_f32_16x16x32_bf16 v[10:13], v[166:169], v[202:205], v[10:13]
	v_mfma_f32_16x16x32_bf16 v[62:65], v[162:165], v[178:181], v[62:65]
	v_mfma_f32_16x16x32_bf16 v[58:61], v[170:173], v[178:181], v[58:61]
	v_mfma_f32_16x16x32_bf16 v[46:49], v[162:165], v[186:189], v[46:49]
	v_mfma_f32_16x16x32_bf16 v[42:45], v[170:173], v[186:189], v[42:45]
	v_mfma_f32_16x16x32_bf16 v[30:33], v[162:165], v[198:201], v[30:33]
	v_mfma_f32_16x16x32_bf16 v[26:29], v[170:173], v[198:201], v[26:29]
	v_mfma_f32_16x16x32_bf16 v[14:17], v[162:165], v[206:209], v[14:17]
	v_mfma_f32_16x16x32_bf16 v[10:13], v[170:173], v[206:209], v[10:13]
	s_barrier
	s_add_u32 s0, s64, 0x40000
	s_addc_u32 s1, s65, 0
	s_add_i32 s33, s36, s38
	s_mov_b32 m0, s33
	s_nop 0
	global_load_lds_dwordx4 v132, s[0:1]
	s_add_i32 m0, s33, 0x2000
	s_nop 0
	global_load_lds_dwordx4 v136, s[0:1]
	v_add_u32_e32 v170, 0x18000, v158
	ds_read_b128 v[152:155], v170
	ds_read_b128 v[162:165], v170 offset:1024
	ds_read_b128 v[166:169], v170 offset:2048
	ds_read_b128 v[170:173], v170 offset:3072
	s_waitcnt vmcnt(6)
	s_barrier
	v_mfma_f32_16x16x32_bf16 v[54:57], v[210:213], v[174:177], v[54:57]
	v_mfma_f32_16x16x32_bf16 v[50:53], v[218:221], v[174:177], v[50:53]
	v_mfma_f32_16x16x32_bf16 v[38:41], v[210:213], v[182:185], v[38:41]
	v_mfma_f32_16x16x32_bf16 v[34:37], v[218:221], v[182:185], v[34:37]
	v_mfma_f32_16x16x32_bf16 v[22:25], v[210:213], v[190:193], v[22:25]
	v_mfma_f32_16x16x32_bf16 v[18:21], v[218:221], v[190:193], v[18:21]
	v_mfma_f32_16x16x32_bf16 v[6:9], v[210:213], v[202:205], v[6:9]
	v_mfma_f32_16x16x32_bf16 v[2:5], v[218:221], v[202:205], v[2:5]
	v_mfma_f32_16x16x32_bf16 v[54:57], v[214:217], v[178:181], v[54:57]
	v_mfma_f32_16x16x32_bf16 v[50:53], v[238:241], v[178:181], v[50:53]
	v_mfma_f32_16x16x32_bf16 v[38:41], v[214:217], v[186:189], v[38:41]
	v_mfma_f32_16x16x32_bf16 v[34:37], v[238:241], v[186:189], v[34:37]
	v_mfma_f32_16x16x32_bf16 v[22:25], v[214:217], v[198:201], v[22:25]
	v_mfma_f32_16x16x32_bf16 v[18:21], v[238:241], v[198:201], v[18:21]
	v_mfma_f32_16x16x32_bf16 v[6:9], v[214:217], v[206:209], v[6:9]
	v_mfma_f32_16x16x32_bf16 v[2:5], v[238:241], v[206:209], v[2:5]
	s_add_i32 s33, 0, 0x18000
	s_barrier
	s_add_u32 s0, s66, 0x40000
	s_addc_u32 s1, s67, 0
	s_mov_b32 m0, s69
	ds_read_b128 v[174:177], v161 offset:32768
	ds_read_b128 v[178:181], v161 offset:33792
	ds_read_b128 v[182:185], v161 offset:34816
	ds_read_b128 v[186:189], v161 offset:35840
	ds_read_b128 v[190:193], v161 offset:36864
	ds_read_b128 v[198:201], v161 offset:37888
	ds_read_b128 v[202:205], v161 offset:38912
	ds_read_b128 v[206:209], v161 offset:39936
	global_load_lds_dwordx4 v130, s[0:1]
	s_mov_b32 m0, s70
	s_nop 0
	global_load_lds_dwordx4 v134, s[0:1]
	s_waitcnt lgkmcnt(8)
	s_barrier
	s_waitcnt lgkmcnt(0)
	v_mfma_f32_16x16x32_bf16 v[126:129], v[152:155], v[174:177], v[126:129]
	v_mfma_f32_16x16x32_bf16 v[122:125], v[166:169], v[174:177], v[122:125]
	v_mfma_f32_16x16x32_bf16 v[110:113], v[152:155], v[182:185], v[110:113]
	v_mfma_f32_16x16x32_bf16 v[106:109], v[166:169], v[182:185], v[106:109]
	v_mfma_f32_16x16x32_bf16 v[94:97], v[152:155], v[190:193], v[94:97]
	v_mfma_f32_16x16x32_bf16 v[90:93], v[166:169], v[190:193], v[90:93]
	v_mfma_f32_16x16x32_bf16 v[78:81], v[152:155], v[202:205], v[78:81]
	v_mfma_f32_16x16x32_bf16 v[74:77], v[166:169], v[202:205], v[74:77]
	v_mfma_f32_16x16x32_bf16 v[126:129], v[162:165], v[178:181], v[126:129]
	v_mfma_f32_16x16x32_bf16 v[122:125], v[170:173], v[178:181], v[122:125]
	v_mfma_f32_16x16x32_bf16 v[110:113], v[162:165], v[186:189], v[110:113]
	v_mfma_f32_16x16x32_bf16 v[106:109], v[170:173], v[186:189], v[106:109]
	v_mfma_f32_16x16x32_bf16 v[94:97], v[162:165], v[198:201], v[94:97]
	v_mfma_f32_16x16x32_bf16 v[90:93], v[170:173], v[198:201], v[90:93]
	v_mfma_f32_16x16x32_bf16 v[78:81], v[162:165], v[206:209], v[78:81]
	v_mfma_f32_16x16x32_bf16 v[74:77], v[170:173], v[206:209], v[74:77]
	s_barrier
	s_add_i32 s36, 0, 0x1c000
	s_add_i32 s0, s33, s38
	v_add_u32_e32 v194, s36, v158
	v_lshl_add_u64 v[156:157], v[156:157], 0, s[54:55]
	s_mov_b32 m0, s0
	ds_read_b128 v[210:213], v194
	ds_read_b128 v[214:217], v194 offset:1024
	ds_read_b128 v[218:221], v194 offset:2048
	ds_read_b128 v[238:241], v194 offset:3072
	global_load_lds_dwordx4 v[156:157], off
	v_lshl_add_u64 v[156:157], v[242:243], 0, s[54:55]
	s_add_i32 m0, s0, 0x2000
	s_nop 0
	global_load_lds_dwordx4 v[156:157], off
	s_barrier
	s_waitcnt lgkmcnt(0)
	v_mfma_f32_16x16x32_bf16 v[118:121], v[210:213], v[174:177], v[118:121]
	v_mfma_f32_16x16x32_bf16 v[114:117], v[218:221], v[174:177], v[114:117]
	v_mfma_f32_16x16x32_bf16 v[102:105], v[210:213], v[182:185], v[102:105]
	v_mfma_f32_16x16x32_bf16 v[98:101], v[218:221], v[182:185], v[98:101]
	v_mfma_f32_16x16x32_bf16 v[86:89], v[210:213], v[190:193], v[86:89]
	v_mfma_f32_16x16x32_bf16 v[82:85], v[218:221], v[190:193], v[82:85]
	v_mfma_f32_16x16x32_bf16 v[70:73], v[210:213], v[202:205], v[70:73]
	v_mfma_f32_16x16x32_bf16 v[66:69], v[218:221], v[202:205], v[66:69]
	v_mfma_f32_16x16x32_bf16 v[118:121], v[214:217], v[178:181], v[118:121]
	v_mfma_f32_16x16x32_bf16 v[114:117], v[238:241], v[178:181], v[114:117]
	v_mfma_f32_16x16x32_bf16 v[102:105], v[214:217], v[186:189], v[102:105]
	v_mfma_f32_16x16x32_bf16 v[98:101], v[238:241], v[186:189], v[98:101]
	v_mfma_f32_16x16x32_bf16 v[86:89], v[214:217], v[198:201], v[86:89]
	v_mfma_f32_16x16x32_bf16 v[82:85], v[238:241], v[198:201], v[82:85]
	v_mfma_f32_16x16x32_bf16 v[70:73], v[214:217], v[206:209], v[70:73]
	v_mfma_f32_16x16x32_bf16 v[66:69], v[238:241], v[206:209], v[66:69]
	s_mov_b32 m0, s71
	v_lshl_add_u64 v[156:157], v[244:245], 0, s[54:55]
	s_barrier
	ds_read_b128 v[174:177], v161 offset:49152
	ds_read_b128 v[178:181], v161 offset:50176
	ds_read_b128 v[182:185], v161 offset:51200
	ds_read_b128 v[186:189], v161 offset:52224
	ds_read_b128 v[190:193], v161 offset:53248
	ds_read_b128 v[198:201], v161 offset:54272
	ds_read_b128 v[202:205], v161 offset:55296
	ds_read_b128 v[206:209], v161 offset:56320
	global_load_lds_dwordx4 v[156:157], off
	v_lshl_add_u64 v[156:157], v[246:247], 0, s[54:55]
	s_mov_b32 m0, s72
	s_nop 0
	global_load_lds_dwordx4 v[156:157], off
	s_waitcnt vmcnt(10)
	s_barrier
	s_waitcnt lgkmcnt(0)
	v_mfma_f32_16x16x32_bf16 v[62:65], v[152:155], v[174:177], v[62:65]
	v_mfma_f32_16x16x32_bf16 v[58:61], v[166:169], v[174:177], v[58:61]
	v_mfma_f32_16x16x32_bf16 v[46:49], v[152:155], v[182:185], v[46:49]
	v_mfma_f32_16x16x32_bf16 v[42:45], v[166:169], v[182:185], v[42:45]
	v_mfma_f32_16x16x32_bf16 v[30:33], v[152:155], v[190:193], v[30:33]
	v_mfma_f32_16x16x32_bf16 v[26:29], v[166:169], v[190:193], v[26:29]
	v_mfma_f32_16x16x32_bf16 v[14:17], v[152:155], v[202:205], v[14:17]
	v_mfma_f32_16x16x32_bf16 v[10:13], v[166:169], v[202:205], v[10:13]
	v_mfma_f32_16x16x32_bf16 v[62:65], v[162:165], v[178:181], v[62:65]
	v_mfma_f32_16x16x32_bf16 v[58:61], v[170:173], v[178:181], v[58:61]
	v_mfma_f32_16x16x32_bf16 v[46:49], v[162:165], v[186:189], v[46:49]
	v_mfma_f32_16x16x32_bf16 v[42:45], v[170:173], v[186:189], v[42:45]
	v_mfma_f32_16x16x32_bf16 v[30:33], v[162:165], v[198:201], v[30:33]
	v_mfma_f32_16x16x32_bf16 v[26:29], v[170:173], v[198:201], v[26:29]
	v_mfma_f32_16x16x32_bf16 v[14:17], v[162:165], v[206:209], v[14:17]
	v_mfma_f32_16x16x32_bf16 v[10:13], v[170:173], v[206:209], v[10:13]
	s_barrier
	s_add_u32 s0, s64, 0x40080
	s_addc_u32 s1, s65, 0
	s_add_i32 s33, s36, s38
	s_mov_b32 m0, s33
	s_nop 0
	global_load_lds_dwordx4 v132, s[0:1]
	s_add_i32 m0, s33, 0x2000
	s_nop 0
	global_load_lds_dwordx4 v136, s[0:1]
	v_add_u32_e32 v170, 0x10000, v158
	ds_read_b128 v[152:155], v170
	ds_read_b128 v[162:165], v170 offset:1024
	ds_read_b128 v[166:169], v170 offset:2048
	ds_read_b128 v[170:173], v170 offset:3072
	s_waitcnt vmcnt(6)
	s_barrier
	v_mfma_f32_16x16x32_bf16 v[54:57], v[210:213], v[174:177], v[54:57]
	v_mfma_f32_16x16x32_bf16 v[50:53], v[218:221], v[174:177], v[50:53]
	v_mfma_f32_16x16x32_bf16 v[38:41], v[210:213], v[182:185], v[38:41]
	v_mfma_f32_16x16x32_bf16 v[34:37], v[218:221], v[182:185], v[34:37]
	v_mfma_f32_16x16x32_bf16 v[22:25], v[210:213], v[190:193], v[22:25]
	v_mfma_f32_16x16x32_bf16 v[18:21], v[218:221], v[190:193], v[18:21]
	v_mfma_f32_16x16x32_bf16 v[6:9], v[210:213], v[202:205], v[6:9]
	v_mfma_f32_16x16x32_bf16 v[2:5], v[218:221], v[202:205], v[2:5]
	v_mfma_f32_16x16x32_bf16 v[54:57], v[214:217], v[178:181], v[54:57]
	v_mfma_f32_16x16x32_bf16 v[50:53], v[238:241], v[178:181], v[50:53]
	v_mfma_f32_16x16x32_bf16 v[38:41], v[214:217], v[186:189], v[38:41]
	v_mfma_f32_16x16x32_bf16 v[34:37], v[238:241], v[186:189], v[34:37]
	v_mfma_f32_16x16x32_bf16 v[22:25], v[214:217], v[198:201], v[22:25]
	v_mfma_f32_16x16x32_bf16 v[18:21], v[238:241], v[198:201], v[18:21]
	v_mfma_f32_16x16x32_bf16 v[6:9], v[214:217], v[206:209], v[6:9]
	v_mfma_f32_16x16x32_bf16 v[2:5], v[238:241], v[206:209], v[2:5]
	s_add_i32 s79, s79, 2
	s_add_u32 s30, s30, 0x100
	s_addc_u32 s31, s31, 0
	s_add_u32 s77, s77, 0x100
	s_addc_u32 s78, s78, 0
	s_cmp_gt_u32 s79, 13
	s_barrier
	s_cbranch_scc0 .LBB0_389
	s_waitcnt lgkmcnt(0)
	s_lshl_b32 s0, s8, 8
	v_lshl_add_u32 v162, s6, 8, v139
	v_or_b32_e32 v152, s0, v138
	s_addk_i32 s0, 0xf200
	v_ashrrev_i32_e32 v155, 5, v162
	s_lshr_b32 s23, s0, 8
	v_and_b32_e32 v155, -8, v155
	v_add_u32_e32 v156, s23, v155
	v_add_u32_e32 v154, 0xfffffe00, v152
	s_movk_i32 s1, 0x3ff
	v_ashrrev_i32_e32 v157, 31, v156
	v_cmp_lt_u32_e64 s[8:9], s1, v154
	s_movk_i32 s1, 0xdff
	v_ashrrev_i32_e32 v153, 31, v152
	v_lshlrev_b64 v[156:157], 17, v[156:157]
	v_cmp_lt_i32_e64 s[6:7], s1, v152
	v_lshl_add_u64 v[152:153], v[152:153], 1, s[18:19]
	v_lshl_add_u64 v[156:157], s[20:21], 0, v[156:157]
	s_and_saveexec_b64 s[0:1], s[8:9]
	s_xor_b64 s[30:31], exec, s[0:1]
	s_cbranch_execz .LBB0_396
	s_and_saveexec_b64 s[0:1], s[6:7]
	s_xor_b64 s[64:65], exec, s[0:1]
	s_cbranch_execz .LBB0_393
	v_mul_f32_e32 v155, 0xbfb8aa3b, v126
	v_exp_f32_e32 v155, v155
	v_mul_f32_e32 v163, 0xbfb8aa3b, v122
	v_exp_f32_e32 v163, v163
	v_mul_f32_e32 v165, 0xbfb8aa3b, v114
	v_add_f32_e32 v155, 1.0, v155
	v_rcp_f32_e32 v168, v155
	v_add_f32_e32 v155, 1.0, v163
	v_rcp_f32_e32 v170, v155
	v_mul_f32_e32 v155, 0xbfb8aa3b, v127
	v_exp_f32_e32 v155, v155
	v_mul_f32_e32 v163, 0xbfb8aa3b, v123
	v_exp_f32_e32 v163, v163
	v_mul_f32_e32 v164, 0xbfb8aa3b, v118
	v_exp_f32_e32 v166, v165
	v_mul_f32_e32 v165, 0xbfb8aa3b, v119
	v_exp_f32_e32 v164, v164
	v_exp_f32_e32 v165, v165
	v_mul_f32_e32 v167, 0xbfb8aa3b, v115
	v_add_f32_e32 v155, 1.0, v155
	v_rcp_f32_e32 v169, v155
	v_exp_f32_e32 v167, v167
	v_add_f32_e32 v163, 1.0, v163
	v_rcp_f32_e32 v171, v163
	v_pk_add_f32 v[164:165], v[164:165], 1.0 op_sel_hi:[1,0]
	v_mul_f32_e32 v178, 0xbfb8aa3b, v117
	v_rcp_f32_e32 v155, v164
	v_pk_mul_f32 v[168:169], v[168:169], v[164:165]
	v_rcp_f32_e32 v163, v165
	v_pk_add_f32 v[164:165], v[166:167], 1.0 op_sel_hi:[1,0]
	s_nop 0
	v_rcp_f32_e32 v176, v164
	v_pk_mul_f32 v[166:167], v[170:171], v[164:165]
	v_mul_f32_e32 v164, 0xbfb8aa3b, v128
	v_rcp_f32_e32 v177, v165
	v_exp_f32_e32 v165, v164
	v_mul_f32_e32 v164, 0xbfb8aa3b, v124
	v_exp_f32_e32 v171, v164
	v_mul_f32_e32 v164, 0xbfb8aa3b, v120
	v_add_f32_e32 v165, 1.0, v165
	v_rcp_f32_e32 v172, v165
	v_add_f32_e32 v165, 1.0, v171
	v_rcp_f32_e32 v174, v165
	v_mul_f32_e32 v165, 0xbfb8aa3b, v129
	v_exp_f32_e32 v171, v165
	v_mul_f32_e32 v165, 0xbfb8aa3b, v125
	v_exp_f32_e32 v175, v165
	v_mul_f32_e32 v165, 0xbfb8aa3b, v121
	v_exp_f32_e32 v164, v164
	v_exp_f32_e32 v165, v165
	v_add_f32_e32 v171, 1.0, v171
	v_rcp_f32_e32 v173, v171
	v_mul_f32_e32 v170, 0xbfb8aa3b, v116
	v_exp_f32_e32 v170, v170
	v_exp_f32_e32 v171, v178
	v_pk_add_f32 v[164:165], v[164:165], 1.0 op_sel_hi:[1,0]
	v_cvt_pk_bf16_f32 v166, v166, v167
	v_rcp_f32_e32 v178, v164
	v_pk_mul_f32 v[172:173], v[172:173], v[164:165]
	v_add_f32_e32 v164, 1.0, v175
	v_rcp_f32_e32 v175, v164
	v_rcp_f32_e32 v179, v165
	v_pk_add_f32 v[164:165], v[170:171], 1.0 op_sel_hi:[1,0]
	s_nop 0
	v_rcp_f32_e32 v180, v164
	v_rcp_f32_e32 v181, v165
	v_pk_mul_f32 v[170:171], v[174:175], v[164:165]
	v_lshl_add_u64 v[174:175], v[140:141], 1, v[156:157]
	v_cvt_pk_bf16_f32 v164, v168, v169
	v_cvt_pk_bf16_f32 v165, v172, v173
	v_cvt_pk_bf16_f32 v167, v170, v171
	v_add_co_u32_e32 v168, vcc, 0x10000, v174
	global_store_dwordx4 v[174:175], v[164:167], off
	s_nop 0
	v_addc_co_u32_e32 v169, vcc, 0, v175, vcc
	v_cvt_pk_bf16_f32 v164, v155, v163
	v_cvt_pk_bf16_f32 v165, v178, v179
	v_cvt_pk_bf16_f32 v166, v176, v177
	v_cvt_pk_bf16_f32 v167, v180, v181
	global_store_dwordx4 v[168:169], v[164:167], off

.LBB0_475:
	s_add_u32 s0, s30, 0xfffc0080
	s_addc_u32 s1, s31, -1
	s_add_i32 s33, 0, 0x10000
	s_cmp_eq_u32 s79, 12
	s_cselect_b32 s67, s5, s1
	s_cselect_b32 s66, s7, s0
	s_cselect_b32 s65, s9, s78
	s_cselect_b32 s64, s23, s77
	s_add_i32 m0, s40, 0xc000
	ds_read_b128 v[174:177], v161
	ds_read_b128 v[178:181], v161 offset:1024
	ds_read_b128 v[182:185], v161 offset:2048
	ds_read_b128 v[186:189], v161 offset:3072
	ds_read_b128 v[190:193], v161 offset:4096
	ds_read_b128 v[198:201], v161 offset:5120
	ds_read_b128 v[202:205], v161 offset:6144
	ds_read_b128 v[206:209], v161 offset:7168
	global_load_lds_dwordx4 v148, s[30:31]
	s_add_i32 m0, s40, 0xe000
	s_nop 0
	global_load_lds_dwordx4 v150, s[30:31]
	s_waitcnt lgkmcnt(8)
	s_barrier
	s_waitcnt lgkmcnt(0)
	v_mfma_f32_16x16x32_bf16 v[126:129], v[152:155], v[174:177], v[126:129]
	v_mfma_f32_16x16x32_bf16 v[122:125], v[166:169], v[174:177], v[122:125]
	v_mfma_f32_16x16x32_bf16 v[110:113], v[152:155], v[182:185], v[110:113]
	v_mfma_f32_16x16x32_bf16 v[106:109], v[166:169], v[182:185], v[106:109]
	v_mfma_f32_16x16x32_bf16 v[94:97], v[152:155], v[190:193], v[94:97]
	v_mfma_f32_16x16x32_bf16 v[90:93], v[166:169], v[190:193], v[90:93]
	v_mfma_f32_16x16x32_bf16 v[78:81], v[152:155], v[202:205], v[78:81]
	v_mfma_f32_16x16x32_bf16 v[74:77], v[166:169], v[202:205], v[74:77]
	v_mfma_f32_16x16x32_bf16 v[126:129], v[162:165], v[178:181], v[126:129]
	v_mfma_f32_16x16x32_bf16 v[122:125], v[170:173], v[178:181], v[122:125]
	v_mfma_f32_16x16x32_bf16 v[110:113], v[162:165], v[186:189], v[110:113]
	v_mfma_f32_16x16x32_bf16 v[106:109], v[170:173], v[186:189], v[106:109]
	v_mfma_f32_16x16x32_bf16 v[94:97], v[162:165], v[198:201], v[94:97]
	v_mfma_f32_16x16x32_bf16 v[90:93], v[170:173], v[198:201], v[90:93]
	v_mfma_f32_16x16x32_bf16 v[78:81], v[162:165], v[206:209], v[78:81]
	v_mfma_f32_16x16x32_bf16 v[74:77], v[170:173], v[206:209], v[74:77]
	s_barrier
	s_add_i32 s36, 0, 0x14000
	v_add_u32_e32 v156, s36, v158
	s_add_i32 s0, s33, s38
	ds_read_b128 v[210:213], v156
	ds_read_b128 v[214:217], v156 offset:1024
	ds_read_b128 v[218:221], v156 offset:2048
	ds_read_b128 v[238:241], v156 offset:3072
	v_lshl_add_u64 v[156:157], s[64:65], 0, v[132:133]
	s_mov_b32 m0, s0
	v_lshl_add_u64 v[242:243], s[64:65], 0, v[136:137]
	global_load_lds_dwordx4 v[156:157], off
	s_add_i32 m0, s0, 0x2000
	s_nop 0
	global_load_lds_dwordx4 v[242:243], off
	s_barrier
	s_waitcnt lgkmcnt(0)
	v_mfma_f32_16x16x32_bf16 v[118:121], v[210:213], v[174:177], v[118:121]
	v_mfma_f32_16x16x32_bf16 v[114:117], v[218:221], v[174:177], v[114:117]
	v_mfma_f32_16x16x32_bf16 v[102:105], v[210:213], v[182:185], v[102:105]
	v_mfma_f32_16x16x32_bf16 v[98:101], v[218:221], v[182:185], v[98:101]
	v_mfma_f32_16x16x32_bf16 v[86:89], v[210:213], v[190:193], v[86:89]
	v_mfma_f32_16x16x32_bf16 v[82:85], v[218:221], v[190:193], v[82:85]
	v_mfma_f32_16x16x32_bf16 v[70:73], v[210:213], v[202:205], v[70:73]
	v_mfma_f32_16x16x32_bf16 v[66:69], v[218:221], v[202:205], v[66:69]
	v_mfma_f32_16x16x32_bf16 v[118:121], v[214:217], v[178:181], v[118:121]
	v_mfma_f32_16x16x32_bf16 v[114:117], v[238:241], v[178:181], v[114:117]
	v_mfma_f32_16x16x32_bf16 v[102:105], v[214:217], v[186:189], v[102:105]
	v_mfma_f32_16x16x32_bf16 v[98:101], v[238:241], v[186:189], v[98:101]
	v_mfma_f32_16x16x32_bf16 v[86:89], v[214:217], v[198:201], v[86:89]
	v_mfma_f32_16x16x32_bf16 v[82:85], v[238:241], v[198:201], v[82:85]
	v_mfma_f32_16x16x32_bf16 v[70:73], v[214:217], v[206:209], v[70:73]
	v_mfma_f32_16x16x32_bf16 v[66:69], v[238:241], v[206:209], v[66:69]
	s_mov_b32 m0, s40
	v_lshl_add_u64 v[244:245], s[66:67], 0, v[130:131]
	s_barrier
	ds_read_b128 v[174:177], v161 offset:16384
	ds_read_b128 v[178:181], v161 offset:17408
	ds_read_b128 v[182:185], v161 offset:18432
	ds_read_b128 v[186:189], v161 offset:19456
	ds_read_b128 v[190:193], v161 offset:20480
	ds_read_b128 v[198:201], v161 offset:21504
	ds_read_b128 v[202:205], v161 offset:22528
	ds_read_b128 v[206:209], v161 offset:23552
	global_load_lds_dwordx4 v[244:245], off
	v_lshl_add_u64 v[246:247], s[66:67], 0, v[134:135]
	s_mov_b32 m0, s43
	s_nop 0
	global_load_lds_dwordx4 v[246:247], off
	s_waitcnt vmcnt(10)
	s_barrier
	s_waitcnt lgkmcnt(0)
	v_mfma_f32_16x16x32_bf16 v[62:65], v[152:155], v[174:177], v[62:65]
	v_mfma_f32_16x16x32_bf16 v[58:61], v[166:169], v[174:177], v[58:61]
	v_mfma_f32_16x16x32_bf16 v[46:49], v[152:155], v[182:185], v[46:49]
	v_mfma_f32_16x16x32_bf16 v[42:45], v[166:169], v[182:185], v[42:45]
	v_mfma_f32_16x16x32_bf16 v[30:33], v[152:155], v[190:193], v[30:33]
	v_mfma_f32_16x16x32_bf16 v[26:29], v[166:169], v[190:193], v[26:29]
	v_mfma_f32_16x16x32_bf16 v[14:17], v[152:155], v[202:205], v[14:17]
	v_mfma_f32_16x16x32_bf16 v[10:13], v[166:169], v[202:205], v[10:13]
	v_mfma_f32_16x16x32_bf16 v[62:65], v[162:165], v[178:181], v[62:65]
	v_mfma_f32_16x16x32_bf16 v[58:61], v[170:173], v[178:181], v[58:61]
	v_mfma_f32_16x16x32_bf16 v[46:49], v[162:165], v[186:189], v[46:49]
	v_mfma_f32_16x16x32_bf16 v[42:45], v[170:173], v[186:189], v[42:45]
	v_mfma_f32_16x16x32_bf16 v[30:33], v[162:165], v[198:201], v[30:33]
	v_mfma_f32_16x16x32_bf16 v[26:29], v[170:173], v[198:201], v[26:29]
	v_mfma_f32_16x16x32_bf16 v[14:17], v[162:165], v[206:209], v[14:17]
	v_mfma_f32_16x16x32_bf16 v[10:13], v[170:173], v[206:209], v[10:13]
	s_barrier
	s_add_u32 s0, s64, 0x40000
	s_addc_u32 s1, s65, 0
	s_add_i32 s33, s36, s38
	s_mov_b32 m0, s33
	s_nop 0
	global_load_lds_dwordx4 v132, s[0:1]
	s_add_i32 m0, s33, 0x2000
	s_nop 0
	global_load_lds_dwordx4 v136, s[0:1]
	v_add_u32_e32 v170, 0x18000, v158
	ds_read_b128 v[152:155], v170
	ds_read_b128 v[162:165], v170 offset:1024
	ds_read_b128 v[166:169], v170 offset:2048
	ds_read_b128 v[170:173], v170 offset:3072
	s_waitcnt vmcnt(6)
	s_barrier
	v_mfma_f32_16x16x32_bf16 v[54:57], v[210:213], v[174:177], v[54:57]
	v_mfma_f32_16x16x32_bf16 v[50:53], v[218:221], v[174:177], v[50:53]
	v_mfma_f32_16x16x32_bf16 v[38:41], v[210:213], v[182:185], v[38:41]
	v_mfma_f32_16x16x32_bf16 v[34:37], v[218:221], v[182:185], v[34:37]
	v_mfma_f32_16x16x32_bf16 v[22:25], v[210:213], v[190:193], v[22:25]
	v_mfma_f32_16x16x32_bf16 v[18:21], v[218:221], v[190:193], v[18:21]
	v_mfma_f32_16x16x32_bf16 v[6:9], v[210:213], v[202:205], v[6:9]
	v_mfma_f32_16x16x32_bf16 v[2:5], v[218:221], v[202:205], v[2:5]
	v_mfma_f32_16x16x32_bf16 v[54:57], v[214:217], v[178:181], v[54:57]
	v_mfma_f32_16x16x32_bf16 v[50:53], v[238:241], v[178:181], v[50:53]
	v_mfma_f32_16x16x32_bf16 v[38:41], v[214:217], v[186:189], v[38:41]
	v_mfma_f32_16x16x32_bf16 v[34:37], v[238:241], v[186:189], v[34:37]
	v_mfma_f32_16x16x32_bf16 v[22:25], v[214:217], v[198:201], v[22:25]
	v_mfma_f32_16x16x32_bf16 v[18:21], v[238:241], v[198:201], v[18:21]
	v_mfma_f32_16x16x32_bf16 v[6:9], v[214:217], v[206:209], v[6:9]
	v_mfma_f32_16x16x32_bf16 v[2:5], v[238:241], v[206:209], v[2:5]
	s_add_i32 s33, 0, 0x18000
	s_barrier
	s_add_u32 s0, s66, 0x40000
	s_addc_u32 s1, s67, 0
	s_mov_b32 m0, s69
	ds_read_b128 v[174:177], v161 offset:32768
	ds_read_b128 v[178:181], v161 offset:33792
	ds_read_b128 v[182:185], v161 offset:34816
	ds_read_b128 v[186:189], v161 offset:35840
	ds_read_b128 v[190:193], v161 offset:36864
	ds_read_b128 v[198:201], v161 offset:37888
	ds_read_b128 v[202:205], v161 offset:38912
	ds_read_b128 v[206:209], v161 offset:39936
	global_load_lds_dwordx4 v130, s[0:1]
	s_mov_b32 m0, s70
	s_nop 0
	global_load_lds_dwordx4 v134, s[0:1]
	s_waitcnt lgkmcnt(8)
	s_barrier
	s_waitcnt lgkmcnt(0)
	v_mfma_f32_16x16x32_bf16 v[126:129], v[152:155], v[174:177], v[126:129]
	v_mfma_f32_16x16x32_bf16 v[122:125], v[166:169], v[174:177], v[122:125]
	v_mfma_f32_16x16x32_bf16 v[110:113], v[152:155], v[182:185], v[110:113]
	v_mfma_f32_16x16x32_bf16 v[106:109], v[166:169], v[182:185], v[106:109]
	v_mfma_f32_16x16x32_bf16 v[94:97], v[152:155], v[190:193], v[94:97]
	v_mfma_f32_16x16x32_bf16 v[90:93], v[166:169], v[190:193], v[90:93]
	v_mfma_f32_16x16x32_bf16 v[78:81], v[152:155], v[202:205], v[78:81]
	v_mfma_f32_16x16x32_bf16 v[74:77], v[166:169], v[202:205], v[74:77]
	v_mfma_f32_16x16x32_bf16 v[126:129], v[162:165], v[178:181], v[126:129]
	v_mfma_f32_16x16x32_bf16 v[122:125], v[170:173], v[178:181], v[122:125]
	v_mfma_f32_16x16x32_bf16 v[110:113], v[162:165], v[186:189], v[110:113]
	v_mfma_f32_16x16x32_bf16 v[106:109], v[170:173], v[186:189], v[106:109]
	v_mfma_f32_16x16x32_bf16 v[94:97], v[162:165], v[198:201], v[94:97]
	v_mfma_f32_16x16x32_bf16 v[90:93], v[170:173], v[198:201], v[90:93]
	v_mfma_f32_16x16x32_bf16 v[78:81], v[162:165], v[206:209], v[78:81]
	v_mfma_f32_16x16x32_bf16 v[74:77], v[170:173], v[206:209], v[74:77]
	s_barrier
	s_add_i32 s36, 0, 0x1c000
	s_add_i32 s0, s33, s38
	v_add_u32_e32 v194, s36, v158
	v_lshl_add_u64 v[156:157], v[156:157], 0, s[54:55]
	s_mov_b32 m0, s0
	ds_read_b128 v[210:213], v194
	ds_read_b128 v[214:217], v194 offset:1024
	ds_read_b128 v[218:221], v194 offset:2048
	ds_read_b128 v[238:241], v194 offset:3072
	global_load_lds_dwordx4 v[156:157], off
	v_lshl_add_u64 v[156:157], v[242:243], 0, s[54:55]
	s_add_i32 m0, s0, 0x2000
	s_nop 0
	global_load_lds_dwordx4 v[156:157], off
	s_barrier
	s_waitcnt lgkmcnt(0)
	v_mfma_f32_16x16x32_bf16 v[118:121], v[210:213], v[174:177], v[118:121]
	v_mfma_f32_16x16x32_bf16 v[114:117], v[218:221], v[174:177], v[114:117]
	v_mfma_f32_16x16x32_bf16 v[102:105], v[210:213], v[182:185], v[102:105]
	v_mfma_f32_16x16x32_bf16 v[98:101], v[218:221], v[182:185], v[98:101]
	v_mfma_f32_16x16x32_bf16 v[86:89], v[210:213], v[190:193], v[86:89]
	v_mfma_f32_16x16x32_bf16 v[82:85], v[218:221], v[190:193], v[82:85]
	v_mfma_f32_16x16x32_bf16 v[70:73], v[210:213], v[202:205], v[70:73]
	v_mfma_f32_16x16x32_bf16 v[66:69], v[218:221], v[202:205], v[66:69]
	v_mfma_f32_16x16x32_bf16 v[118:121], v[214:217], v[178:181], v[118:121]
	v_mfma_f32_16x16x32_bf16 v[114:117], v[238:241], v[178:181], v[114:117]
	v_mfma_f32_16x16x32_bf16 v[102:105], v[214:217], v[186:189], v[102:105]
	v_mfma_f32_16x16x32_bf16 v[98:101], v[238:241], v[186:189], v[98:101]
	v_mfma_f32_16x16x32_bf16 v[86:89], v[214:217], v[198:201], v[86:89]
	v_mfma_f32_16x16x32_bf16 v[82:85], v[238:241], v[198:201], v[82:85]
	v_mfma_f32_16x16x32_bf16 v[70:73], v[214:217], v[206:209], v[70:73]
	v_mfma_f32_16x16x32_bf16 v[66:69], v[238:241], v[206:209], v[66:69]
	s_mov_b32 m0, s71
	v_lshl_add_u64 v[156:157], v[244:245], 0, s[54:55]
	s_barrier
	ds_read_b128 v[174:177], v161 offset:49152
	ds_read_b128 v[178:181], v161 offset:50176
	ds_read_b128 v[182:185], v161 offset:51200
	ds_read_b128 v[186:189], v161 offset:52224
	ds_read_b128 v[190:193], v161 offset:53248
	ds_read_b128 v[198:201], v161 offset:54272
	ds_read_b128 v[202:205], v161 offset:55296
	ds_read_b128 v[206:209], v161 offset:56320
	global_load_lds_dwordx4 v[156:157], off
	v_lshl_add_u64 v[156:157], v[246:247], 0, s[54:55]
	s_mov_b32 m0, s72
	s_nop 0
	global_load_lds_dwordx4 v[156:157], off
	s_waitcnt vmcnt(10)
	s_barrier
	s_waitcnt lgkmcnt(0)
	v_mfma_f32_16x16x32_bf16 v[62:65], v[152:155], v[174:177], v[62:65]
	v_mfma_f32_16x16x32_bf16 v[58:61], v[166:169], v[174:177], v[58:61]
	v_mfma_f32_16x16x32_bf16 v[46:49], v[152:155], v[182:185], v[46:49]
	v_mfma_f32_16x16x32_bf16 v[42:45], v[166:169], v[182:185], v[42:45]
	v_mfma_f32_16x16x32_bf16 v[30:33], v[152:155], v[190:193], v[30:33]
	v_mfma_f32_16x16x32_bf16 v[26:29], v[166:169], v[190:193], v[26:29]
	v_mfma_f32_16x16x32_bf16 v[14:17], v[152:155], v[202:205], v[14:17]
	v_mfma_f32_16x16x32_bf16 v[10:13], v[166:169], v[202:205], v[10:13]
	v_mfma_f32_16x16x32_bf16 v[62:65], v[162:165], v[178:181], v[62:65]
	v_mfma_f32_16x16x32_bf16 v[58:61], v[170:173], v[178:181], v[58:61]
	v_mfma_f32_16x16x32_bf16 v[46:49], v[162:165], v[186:189], v[46:49]
	v_mfma_f32_16x16x32_bf16 v[42:45], v[170:173], v[186:189], v[42:45]
	v_mfma_f32_16x16x32_bf16 v[30:33], v[162:165], v[198:201], v[30:33]
	v_mfma_f32_16x16x32_bf16 v[26:29], v[170:173], v[198:201], v[26:29]
	v_mfma_f32_16x16x32_bf16 v[14:17], v[162:165], v[206:209], v[14:17]
	v_mfma_f32_16x16x32_bf16 v[10:13], v[170:173], v[206:209], v[10:13]
	s_barrier
	s_add_u32 s0, s64, 0x40080
	s_addc_u32 s1, s65, 0
	s_add_i32 s33, s36, s38
	s_mov_b32 m0, s33
	s_nop 0
	global_load_lds_dwordx4 v132, s[0:1]
	s_add_i32 m0, s33, 0x2000
	s_nop 0
	global_load_lds_dwordx4 v136, s[0:1]
	v_add_u32_e32 v170, 0x10000, v158
	ds_read_b128 v[152:155], v170
	ds_read_b128 v[162:165], v170 offset:1024
	ds_read_b128 v[166:169], v170 offset:2048
	ds_read_b128 v[170:173], v170 offset:3072
	s_waitcnt vmcnt(6)
	s_barrier
	v_mfma_f32_16x16x32_bf16 v[54:57], v[210:213], v[174:177], v[54:57]
	v_mfma_f32_16x16x32_bf16 v[50:53], v[218:221], v[174:177], v[50:53]
	v_mfma_f32_16x16x32_bf16 v[38:41], v[210:213], v[182:185], v[38:41]
	v_mfma_f32_16x16x32_bf16 v[34:37], v[218:221], v[182:185], v[34:37]
	v_mfma_f32_16x16x32_bf16 v[22:25], v[210:213], v[190:193], v[22:25]
	v_mfma_f32_16x16x32_bf16 v[18:21], v[218:221], v[190:193], v[18:21]
	v_mfma_f32_16x16x32_bf16 v[6:9], v[210:213], v[202:205], v[6:9]
	v_mfma_f32_16x16x32_bf16 v[2:5], v[218:221], v[202:205], v[2:5]
	v_mfma_f32_16x16x32_bf16 v[54:57], v[214:217], v[178:181], v[54:57]
	v_mfma_f32_16x16x32_bf16 v[50:53], v[238:241], v[178:181], v[50:53]
	v_mfma_f32_16x16x32_bf16 v[38:41], v[214:217], v[186:189], v[38:41]
	v_mfma_f32_16x16x32_bf16 v[34:37], v[238:241], v[186:189], v[34:37]
	v_mfma_f32_16x16x32_bf16 v[22:25], v[214:217], v[198:201], v[22:25]
	v_mfma_f32_16x16x32_bf16 v[18:21], v[238:241], v[198:201], v[18:21]
	v_mfma_f32_16x16x32_bf16 v[6:9], v[214:217], v[206:209], v[6:9]
	v_mfma_f32_16x16x32_bf16 v[2:5], v[238:241], v[206:209], v[2:5]
	s_add_i32 s79, s79, 2
	s_add_u32 s30, s30, 0x100
	s_addc_u32 s31, s31, 0
	s_add_u32 s77, s77, 0x100
	s_addc_u32 s78, s78, 0
	s_cmp_gt_u32 s79, 13
	s_barrier
	s_cbranch_scc0 .LBB0_475
	s_waitcnt lgkmcnt(0)
	s_lshl_b32 s0, s6, 8
	v_lshl_add_u32 v162, s4, 8, v139
	v_or_b32_e32 v152, s0, v138
	s_addk_i32 s0, 0xf200
	v_ashrrev_i32_e32 v155, 5, v162
	s_lshr_b32 s9, s0, 8
	v_and_b32_e32 v155, -8, v155
	v_add_u32_e32 v154, 0xfffffe00, v152
	s_movk_i32 s1, 0x3ff
	v_add_u32_e32 v156, s9, v155
	v_cmp_lt_u32_e64 s[6:7], s1, v154
	s_movk_i32 s1, 0xdff
	v_ashrrev_i32_e32 v157, 31, v156
	v_cmp_lt_i32_e64 s[4:5], s1, v152
	v_ashrrev_i32_e32 v153, 31, v152
	v_lshlrev_b64 v[156:157], 17, v[156:157]
	s_and_saveexec_b64 s[0:1], s[6:7]
	s_xor_b64 s[30:31], exec, s[0:1]
	s_cbranch_execz .LBB0_482
	s_and_saveexec_b64 s[0:1], s[4:5]
	s_xor_b64 s[64:65], exec, s[0:1]
	s_cbranch_execz .LBB0_479
	v_mul_f32_e32 v155, 0xbfb8aa3b, v126
	v_exp_f32_e32 v155, v155
	v_mul_f32_e32 v163, 0xbfb8aa3b, v122
	v_exp_f32_e32 v163, v163
	v_mul_f32_e32 v165, 0xbfb8aa3b, v114
	v_add_f32_e32 v155, 1.0, v155
	v_rcp_f32_e32 v168, v155
	v_add_f32_e32 v155, 1.0, v163
	v_rcp_f32_e32 v170, v155
	v_mul_f32_e32 v155, 0xbfb8aa3b, v127
	v_exp_f32_e32 v155, v155
	v_mul_f32_e32 v163, 0xbfb8aa3b, v123
	v_exp_f32_e32 v163, v163
	v_mul_f32_e32 v164, 0xbfb8aa3b, v118
	v_exp_f32_e32 v166, v165
	v_mul_f32_e32 v165, 0xbfb8aa3b, v119
	v_exp_f32_e32 v164, v164
	v_exp_f32_e32 v165, v165
	v_mul_f32_e32 v167, 0xbfb8aa3b, v115
	v_add_f32_e32 v155, 1.0, v155
	v_rcp_f32_e32 v169, v155
	v_exp_f32_e32 v167, v167
	v_add_f32_e32 v163, 1.0, v163
	v_rcp_f32_e32 v171, v163
	v_pk_add_f32 v[164:165], v[164:165], 1.0 op_sel_hi:[1,0]
	v_mul_f32_e32 v178, 0xbfb8aa3b, v117
	v_rcp_f32_e32 v155, v164
	v_pk_mul_f32 v[168:169], v[168:169], v[164:165]
	v_rcp_f32_e32 v163, v165
	v_pk_add_f32 v[164:165], v[166:167], 1.0 op_sel_hi:[1,0]
	s_nop 0
	v_rcp_f32_e32 v176, v164
	v_pk_mul_f32 v[166:167], v[170:171], v[164:165]
	v_mul_f32_e32 v164, 0xbfb8aa3b, v128
	v_rcp_f32_e32 v177, v165
	v_exp_f32_e32 v165, v164
	v_mul_f32_e32 v164, 0xbfb8aa3b, v124
	v_exp_f32_e32 v171, v164
	v_mul_f32_e32 v164, 0xbfb8aa3b, v120
	v_add_f32_e32 v165, 1.0, v165
	v_rcp_f32_e32 v172, v165
	v_add_f32_e32 v165, 1.0, v171
	v_rcp_f32_e32 v174, v165
	v_mul_f32_e32 v165, 0xbfb8aa3b, v129
	v_exp_f32_e32 v171, v165
	v_mul_f32_e32 v165, 0xbfb8aa3b, v125
	v_exp_f32_e32 v175, v165
	v_mul_f32_e32 v165, 0xbfb8aa3b, v121
	v_exp_f32_e32 v164, v164
	v_exp_f32_e32 v165, v165
	v_add_f32_e32 v171, 1.0, v171
	v_rcp_f32_e32 v173, v171
	v_mul_f32_e32 v170, 0xbfb8aa3b, v116
	v_exp_f32_e32 v170, v170
	v_exp_f32_e32 v171, v178
	v_pk_add_f32 v[164:165], v[164:165], 1.0 op_sel_hi:[1,0]
	v_cvt_pk_bf16_f32 v166, v166, v167
	v_rcp_f32_e32 v178, v164
	v_pk_mul_f32 v[172:173], v[172:173], v[164:165]
	v_add_f32_e32 v164, 1.0, v175
	v_rcp_f32_e32 v175, v164
	v_rcp_f32_e32 v179, v165
	v_pk_add_f32 v[164:165], v[170:171], 1.0 op_sel_hi:[1,0]
	s_nop 0
	v_rcp_f32_e32 v180, v164
	v_rcp_f32_e32 v181, v165
	v_pk_mul_f32 v[170:171], v[174:175], v[164:165]
	v_lshl_add_u64 v[174:175], v[140:141], 0, v[156:157]
	v_cvt_pk_bf16_f32 v164, v168, v169
	v_cvt_pk_bf16_f32 v165, v172, v173
	v_cvt_pk_bf16_f32 v167, v170, v171
	v_add_co_u32_e32 v168, vcc, 0x10000, v174
	global_store_dwordx4 v[174:175], v[164:167], off
	s_nop 0
	v_addc_co_u32_e32 v169, vcc, 0, v175, vcc
	v_cvt_pk_bf16_f32 v164, v155, v163
	v_cvt_pk_bf16_f32 v165, v178, v179
	v_cvt_pk_bf16_f32 v166, v176, v177
	v_cvt_pk_bf16_f32 v167, v180, v181
	global_store_dwordx4 v[168:169], v[164:167], off
